# qk-norm bound units: coalesced row reads (8 lanes per 128-byte row, 8 rows per load, all 16 loads in flight), row sums by DPP adds
# baseline (speedup 1.0000x reference)
; DI void refresh(Frame& F) { int t_ = F.tid; asm volatile("" : "+v"(t_)); F.tid = t_; F.lane = t_ & 63; F.wave = __builtin_amdgcn_readfirstlane(t_ >> 6); size_t z_ = 0; unsigned zl_ = 0; asm volatile("" : "+s"(z_), "+s"(zl_)); F.ws = F.ws + z_; F.lds = F.lds + zl_; }
; DI void qknorm_unit(Frame& F, int u, gu32* qkn) {
;     refresh(F);
;     const int bh = u >> 4, seg = u & 15, b = bh >> 2, h = bh & 3;
;     const bf16* proj = (const bf16*)(F.ws + WS_PROJ);
;     float qm = 0.f, km = 0.f;
; #pragma unroll
;     for (int i = 0; i < 1; ++i) { const size_t row = (size_t)b * SEQ + seg * 512 + F.tid + i; float qs = 0.f, ks = 0.f;
; #pragma unroll
;         for (int c = 0; c < 8; ++c) { float x[8];
;             unpack8(*(const v4u*)(proj + row * PP + O_AQ + h * 64 + 8 * c), x);
; #pragma unroll
;             for (int e = 0; e < 8; ++e) qs += x[e] * x[e];
;             unpack8(*(const v4u*)(proj + row * PP + O_AK + h * 64 + 8 * c), x);
; #pragma unroll
;             for (int e = 0; e < 8; ++e) ks += x[e] * x[e]; }
;         qm = fmaxf(qm, qs); km = fmaxf(km, ks); }
.LBB0_945:
	s_mov_b64 s[0:1], 0
	s_add_u32 s20, s20, s0
	s_addc_u32 s21, s21, s1
	s_ashr_i32 s0, s26, 6
	s_lshl_b32 s2, s26, 9
	s_lshl_b32 s0, s0, 13
	s_and_b32 s2, s2, 0x1e00
	s_or_b32 s0, s0, s2
	s_ashr_i32 s4, s26, 4
	s_lshl_b32 s1, s4, 7
	s_and_b32 s1, s1, 0x180
	s_mul_hi_u32 s3, s0, s33
	s_mul_i32 s2, s0, s33
	s_add_u32 s2, s2, s1
	s_addc_u32 s3, s3, 0
	s_add_u32 s2, s2, 0xb100000
	s_addc_u32 s3, s3, 0
	s_add_u32 s10, s20, s2
	s_addc_u32 s11, s21, s3
	s_add_u32 s12, s10, 0xd000
	s_addc_u32 s13, s11, 0
	s_add_u32 s14, s12, 0xd000
	s_addc_u32 s15, s13, 0
	s_add_u32 s22, s14, 0xd000
	s_addc_u32 s23, s15, 0
	s_add_u32 s28, s22, 0xd000
	s_addc_u32 s29, s23, 0
	s_add_u32 s34, s28, 0xd000
	s_addc_u32 s35, s29, 0
	s_add_u32 s36, s34, 0xd000
	s_addc_u32 s37, s35, 0
	s_add_u32 s38, s36, 0xd000
	s_addc_u32 s39, s37, 0
	s_waitcnt vmcnt(0) lgkmcnt(0)
	v_and_b32_e32 v1, 63, v132
	v_and_b32_e32 v0, 0xffffffc0, v132
	v_bfe_u32 v2, v132, 3, 3
	v_or_b32_e32 v0, v0, v2
	v_mul_u32_u24_e32 v0, 0x1a00, v0
	v_and_b32_e32 v2, 7, v132
	v_lshl_add_u32 v0, v2, 4, v0
	v_cmp_eq_u32_e32 vcc, 0, v1
	global_load_dwordx4 v[4:7], v0, s[10:11]
	global_load_dwordx4 v[8:11], v0, s[10:11] offset:512
	global_load_dwordx4 v[12:15], v0, s[12:13]
	global_load_dwordx4 v[16:19], v0, s[12:13] offset:512
	global_load_dwordx4 v[20:23], v0, s[14:15]
	global_load_dwordx4 v[24:27], v0, s[14:15] offset:512
	global_load_dwordx4 v[28:31], v0, s[22:23]
	global_load_dwordx4 v[32:35], v0, s[22:23] offset:512
	global_load_dwordx4 v[152:155], v0, s[28:29]
	global_load_dwordx4 v[156:159], v0, s[28:29] offset:512
	global_load_dwordx4 v[160:163], v0, s[34:35]
	global_load_dwordx4 v[164:167], v0, s[34:35] offset:512
	global_load_dwordx4 v[168:171], v0, s[36:37]
	global_load_dwordx4 v[172:175], v0, s[36:37] offset:512
	global_load_dwordx4 v[176:179], v0, s[38:39]
	global_load_dwordx4 v[180:183], v0, s[38:39] offset:512
	s_waitcnt vmcnt(15)
	v_lshlrev_b32_e32 v192, 16, v4
	v_and_b32_e32 v193, 0xffff0000, v4
	v_mul_f32_e32 v36, v192, v192
	v_fmac_f32_e32 v36, v193, v193
	v_lshlrev_b32_e32 v192, 16, v5
	v_and_b32_e32 v193, 0xffff0000, v5
	v_fmac_f32_e32 v36, v192, v192
	v_fmac_f32_e32 v36, v193, v193
	v_lshlrev_b32_e32 v192, 16, v6
	v_and_b32_e32 v193, 0xffff0000, v6
	v_fmac_f32_e32 v36, v192, v192
	v_fmac_f32_e32 v36, v193, v193
	v_lshlrev_b32_e32 v192, 16, v7
	v_and_b32_e32 v193, 0xffff0000, v7
	v_fmac_f32_e32 v36, v192, v192
	v_fmac_f32_e32 v36, v193, v193
	s_waitcnt vmcnt(14)
	v_lshlrev_b32_e32 v194, 16, v8
	v_and_b32_e32 v195, 0xffff0000, v8
	v_mul_f32_e32 v184, v194, v194
	v_fmac_f32_e32 v184, v195, v195
	v_lshlrev_b32_e32 v194, 16, v9
	v_and_b32_e32 v195, 0xffff0000, v9
	v_fmac_f32_e32 v184, v194, v194
	v_fmac_f32_e32 v184, v195, v195
	v_lshlrev_b32_e32 v194, 16, v10
	v_and_b32_e32 v195, 0xffff0000, v10
	v_fmac_f32_e32 v184, v194, v194
	v_fmac_f32_e32 v184, v195, v195
	v_lshlrev_b32_e32 v194, 16, v11
	v_and_b32_e32 v195, 0xffff0000, v11
	v_fmac_f32_e32 v184, v194, v194
	v_fmac_f32_e32 v184, v195, v195
	s_waitcnt vmcnt(13)
	v_lshlrev_b32_e32 v192, 16, v12
	v_and_b32_e32 v193, 0xffff0000, v12
	v_mul_f32_e32 v37, v192, v192
	v_fmac_f32_e32 v37, v193, v193
	v_lshlrev_b32_e32 v192, 16, v13
	v_and_b32_e32 v193, 0xffff0000, v13
	v_fmac_f32_e32 v37, v192, v192
	v_fmac_f32_e32 v37, v193, v193
	v_lshlrev_b32_e32 v192, 16, v14
	v_and_b32_e32 v193, 0xffff0000, v14
	v_fmac_f32_e32 v37, v192, v192
	v_fmac_f32_e32 v37, v193, v193
	v_lshlrev_b32_e32 v192, 16, v15
	v_and_b32_e32 v193, 0xffff0000, v15
	v_fmac_f32_e32 v37, v192, v192
	v_fmac_f32_e32 v37, v193, v193
	s_waitcnt vmcnt(12)
	v_lshlrev_b32_e32 v194, 16, v16
	v_and_b32_e32 v195, 0xffff0000, v16
	v_mul_f32_e32 v185, v194, v194
	v_fmac_f32_e32 v185, v195, v195
	v_lshlrev_b32_e32 v194, 16, v17
	v_and_b32_e32 v195, 0xffff0000, v17
	v_fmac_f32_e32 v185, v194, v194
	v_fmac_f32_e32 v185, v195, v195
	v_lshlrev_b32_e32 v194, 16, v18
	v_and_b32_e32 v195, 0xffff0000, v18
	v_fmac_f32_e32 v185, v194, v194
	v_fmac_f32_e32 v185, v195, v195
	v_lshlrev_b32_e32 v194, 16, v19
	v_and_b32_e32 v195, 0xffff0000, v19
	v_fmac_f32_e32 v185, v194, v194
	v_fmac_f32_e32 v185, v195, v195
	s_waitcnt vmcnt(11)
	v_lshlrev_b32_e32 v192, 16, v20
	v_and_b32_e32 v193, 0xffff0000, v20
	v_mul_f32_e32 v38, v192, v192
	v_fmac_f32_e32 v38, v193, v193
	v_lshlrev_b32_e32 v192, 16, v21
	v_and_b32_e32 v193, 0xffff0000, v21
	v_fmac_f32_e32 v38, v192, v192
	v_fmac_f32_e32 v38, v193, v193
	v_lshlrev_b32_e32 v192, 16, v22
	v_and_b32_e32 v193, 0xffff0000, v22
	v_fmac_f32_e32 v38, v192, v192
	v_fmac_f32_e32 v38, v193, v193
	v_lshlrev_b32_e32 v192, 16, v23
	v_and_b32_e32 v193, 0xffff0000, v23
	v_fmac_f32_e32 v38, v192, v192
	v_fmac_f32_e32 v38, v193, v193
	s_waitcnt vmcnt(10)
	v_lshlrev_b32_e32 v194, 16, v24
	v_and_b32_e32 v195, 0xffff0000, v24
	v_mul_f32_e32 v186, v194, v194
	v_fmac_f32_e32 v186, v195, v195
	v_lshlrev_b32_e32 v194, 16, v25
	v_and_b32_e32 v195, 0xffff0000, v25
	v_fmac_f32_e32 v186, v194, v194
	v_fmac_f32_e32 v186, v195, v195
	v_lshlrev_b32_e32 v194, 16, v26
	v_and_b32_e32 v195, 0xffff0000, v26
	v_fmac_f32_e32 v186, v194, v194
	v_fmac_f32_e32 v186, v195, v195
	v_lshlrev_b32_e32 v194, 16, v27
	v_and_b32_e32 v195, 0xffff0000, v27
	v_fmac_f32_e32 v186, v194, v194
	v_fmac_f32_e32 v186, v195, v195
	s_waitcnt vmcnt(9)
	v_lshlrev_b32_e32 v192, 16, v28
	v_and_b32_e32 v193, 0xffff0000, v28
	v_mul_f32_e32 v39, v192, v192
	v_fmac_f32_e32 v39, v193, v193
	v_lshlrev_b32_e32 v192, 16, v29
	v_and_b32_e32 v193, 0xffff0000, v29
	v_fmac_f32_e32 v39, v192, v192
	v_fmac_f32_e32 v39, v193, v193
	v_lshlrev_b32_e32 v192, 16, v30
	v_and_b32_e32 v193, 0xffff0000, v30
	v_fmac_f32_e32 v39, v192, v192
	v_fmac_f32_e32 v39, v193, v193
	v_lshlrev_b32_e32 v192, 16, v31
	v_and_b32_e32 v193, 0xffff0000, v31
	v_fmac_f32_e32 v39, v192, v192
	v_fmac_f32_e32 v39, v193, v193
	s_waitcnt vmcnt(8)
; DI void qknorm_unit(Frame& F, int u, gu32* qkn) {
;     ...
;     for (int i = 0; i < 1; ++i) { const size_t row = (size_t)b * SEQ + seg * 512 + F.tid + i; float qs = 0.f, ks = 0.f;
; #pragma unroll
;         for (int c = 0; c < 8; ++c) { float x[8];
;             unpack8(*(const v4u*)(proj + row * PP + O_AQ + h * 64 + 8 * c), x);
; #pragma unroll
;             for (int e = 0; e < 8; ++e) qs += x[e] * x[e];
;             unpack8(*(const v4u*)(proj + row * PP + O_AK + h * 64 + 8 * c), x);
; #pragma unroll
;             for (int e = 0; e < 8; ++e) ks += x[e] * x[e]; }
;         qm = fmaxf(qm, qs); km = fmaxf(km, ks); }
	v_lshlrev_b32_e32 v194, 16, v32
	v_and_b32_e32 v195, 0xffff0000, v32
	v_mul_f32_e32 v187, v194, v194
	v_fmac_f32_e32 v187, v195, v195
	v_lshlrev_b32_e32 v194, 16, v33
	v_and_b32_e32 v195, 0xffff0000, v33
	v_fmac_f32_e32 v187, v194, v194
	v_fmac_f32_e32 v187, v195, v195
	v_lshlrev_b32_e32 v194, 16, v34
	v_and_b32_e32 v195, 0xffff0000, v34
	v_fmac_f32_e32 v187, v194, v194
	v_fmac_f32_e32 v187, v195, v195
	v_lshlrev_b32_e32 v194, 16, v35
	v_and_b32_e32 v195, 0xffff0000, v35
	v_fmac_f32_e32 v187, v194, v194
	v_fmac_f32_e32 v187, v195, v195
	s_waitcnt vmcnt(7)
	v_lshlrev_b32_e32 v192, 16, v152
	v_and_b32_e32 v193, 0xffff0000, v152
	v_mul_f32_e32 v40, v192, v192
	v_fmac_f32_e32 v40, v193, v193
	v_lshlrev_b32_e32 v192, 16, v153
	v_and_b32_e32 v193, 0xffff0000, v153
	v_fmac_f32_e32 v40, v192, v192
	v_fmac_f32_e32 v40, v193, v193
	v_lshlrev_b32_e32 v192, 16, v154
	v_and_b32_e32 v193, 0xffff0000, v154
	v_fmac_f32_e32 v40, v192, v192
	v_fmac_f32_e32 v40, v193, v193
	v_lshlrev_b32_e32 v192, 16, v155
	v_and_b32_e32 v193, 0xffff0000, v155
	v_fmac_f32_e32 v40, v192, v192
	v_fmac_f32_e32 v40, v193, v193
	s_waitcnt vmcnt(6)
	v_lshlrev_b32_e32 v194, 16, v156
	v_and_b32_e32 v195, 0xffff0000, v156
	v_mul_f32_e32 v188, v194, v194
	v_fmac_f32_e32 v188, v195, v195
	v_lshlrev_b32_e32 v194, 16, v157
	v_and_b32_e32 v195, 0xffff0000, v157
	v_fmac_f32_e32 v188, v194, v194
	v_fmac_f32_e32 v188, v195, v195
	v_lshlrev_b32_e32 v194, 16, v158
	v_and_b32_e32 v195, 0xffff0000, v158
	v_fmac_f32_e32 v188, v194, v194
	v_fmac_f32_e32 v188, v195, v195
	v_lshlrev_b32_e32 v194, 16, v159
	v_and_b32_e32 v195, 0xffff0000, v159
	v_fmac_f32_e32 v188, v194, v194
	v_fmac_f32_e32 v188, v195, v195
	s_waitcnt vmcnt(5)
	v_lshlrev_b32_e32 v192, 16, v160
	v_and_b32_e32 v193, 0xffff0000, v160
	v_mul_f32_e32 v41, v192, v192
	v_fmac_f32_e32 v41, v193, v193
	v_lshlrev_b32_e32 v192, 16, v161
	v_and_b32_e32 v193, 0xffff0000, v161
	v_fmac_f32_e32 v41, v192, v192
	v_fmac_f32_e32 v41, v193, v193
	v_lshlrev_b32_e32 v192, 16, v162
	v_and_b32_e32 v193, 0xffff0000, v162
	v_fmac_f32_e32 v41, v192, v192
	v_fmac_f32_e32 v41, v193, v193
	v_lshlrev_b32_e32 v192, 16, v163
	v_and_b32_e32 v193, 0xffff0000, v163
	v_fmac_f32_e32 v41, v192, v192
	v_fmac_f32_e32 v41, v193, v193
	s_waitcnt vmcnt(4)
	v_lshlrev_b32_e32 v194, 16, v164
	v_and_b32_e32 v195, 0xffff0000, v164
	v_mul_f32_e32 v189, v194, v194
	v_fmac_f32_e32 v189, v195, v195
	v_lshlrev_b32_e32 v194, 16, v165
	v_and_b32_e32 v195, 0xffff0000, v165
	v_fmac_f32_e32 v189, v194, v194
	v_fmac_f32_e32 v189, v195, v195
	v_lshlrev_b32_e32 v194, 16, v166
	v_and_b32_e32 v195, 0xffff0000, v166
	v_fmac_f32_e32 v189, v194, v194
	v_fmac_f32_e32 v189, v195, v195
	v_lshlrev_b32_e32 v194, 16, v167
	v_and_b32_e32 v195, 0xffff0000, v167
	v_fmac_f32_e32 v189, v194, v194
	v_fmac_f32_e32 v189, v195, v195
	s_waitcnt vmcnt(3)
	v_lshlrev_b32_e32 v192, 16, v168
	v_and_b32_e32 v193, 0xffff0000, v168
	v_mul_f32_e32 v42, v192, v192
	v_fmac_f32_e32 v42, v193, v193
	v_lshlrev_b32_e32 v192, 16, v169
	v_and_b32_e32 v193, 0xffff0000, v169
	v_fmac_f32_e32 v42, v192, v192
	v_fmac_f32_e32 v42, v193, v193
	v_lshlrev_b32_e32 v192, 16, v170
	v_and_b32_e32 v193, 0xffff0000, v170
	v_fmac_f32_e32 v42, v192, v192
	v_fmac_f32_e32 v42, v193, v193
	v_lshlrev_b32_e32 v192, 16, v171
	v_and_b32_e32 v193, 0xffff0000, v171
	v_fmac_f32_e32 v42, v192, v192
	v_fmac_f32_e32 v42, v193, v193
	s_waitcnt vmcnt(2)
	v_lshlrev_b32_e32 v194, 16, v172
	v_and_b32_e32 v195, 0xffff0000, v172
	v_mul_f32_e32 v190, v194, v194
	v_fmac_f32_e32 v190, v195, v195
	v_lshlrev_b32_e32 v194, 16, v173
	v_and_b32_e32 v195, 0xffff0000, v173
	v_fmac_f32_e32 v190, v194, v194
	v_fmac_f32_e32 v190, v195, v195
	v_lshlrev_b32_e32 v194, 16, v174
	v_and_b32_e32 v195, 0xffff0000, v174
	v_fmac_f32_e32 v190, v194, v194
	v_fmac_f32_e32 v190, v195, v195
	v_lshlrev_b32_e32 v194, 16, v175
	v_and_b32_e32 v195, 0xffff0000, v175
	v_fmac_f32_e32 v190, v194, v194
	v_fmac_f32_e32 v190, v195, v195
	s_waitcnt vmcnt(1)
	v_lshlrev_b32_e32 v192, 16, v176
	v_and_b32_e32 v193, 0xffff0000, v176
	v_mul_f32_e32 v43, v192, v192
	v_fmac_f32_e32 v43, v193, v193
	v_lshlrev_b32_e32 v192, 16, v177
	v_and_b32_e32 v193, 0xffff0000, v177
	v_fmac_f32_e32 v43, v192, v192
	v_fmac_f32_e32 v43, v193, v193
	v_lshlrev_b32_e32 v192, 16, v178
	v_and_b32_e32 v193, 0xffff0000, v178
	v_fmac_f32_e32 v43, v192, v192
	v_fmac_f32_e32 v43, v193, v193
	v_lshlrev_b32_e32 v192, 16, v179
	v_and_b32_e32 v193, 0xffff0000, v179
	v_fmac_f32_e32 v43, v192, v192
	v_fmac_f32_e32 v43, v193, v193
	s_waitcnt vmcnt(0)
; DI float shx(float v, int o, int lane) { return __int_as_float(__builtin_amdgcn_ds_bpermute((lane ^ o) << 2, __float_as_int(v))); }
; DI void qknorm_unit(Frame& F, int u, gu32* qkn) {
;     ...
;     for (int i = 0; i < 1; ++i) { const size_t row = (size_t)b * SEQ + seg * 512 + F.tid + i; float qs = 0.f, ks = 0.f;
; #pragma unroll
;         for (int c = 0; c < 8; ++c) { float x[8];
;             unpack8(*(const v4u*)(proj + row * PP + O_AQ + h * 64 + 8 * c), x);
; #pragma unroll
;             for (int e = 0; e < 8; ++e) qs += x[e] * x[e];
;             unpack8(*(const v4u*)(proj + row * PP + O_AK + h * 64 + 8 * c), x);
; #pragma unroll
;             for (int e = 0; e < 8; ++e) ks += x[e] * x[e]; }
;         qm = fmaxf(qm, qs); km = fmaxf(km, ks); }
; #pragma unroll
;     for (int o = 1; o < 64; o <<= 1) { qm = fmaxf(qm, shx(qm, o, F.lane)); km = fmaxf(km, shx(km, o, F.lane)); }
;     if (F.lane == 0) { __hip_atomic_fetch_max(qkn + 2 * bh, __float_as_uint(qm), __ATOMIC_RELAXED, __HIP_MEMORY_SCOPE_AGENT); __hip_atomic_fetch_max(qkn + 2 * bh + 1, __float_as_uint(km), __ATOMIC_RELAXED, __HIP_MEMORY_SCOPE_AGENT); }
; }
	v_lshlrev_b32_e32 v194, 16, v180
	v_and_b32_e32 v195, 0xffff0000, v180
	v_mul_f32_e32 v191, v194, v194
	v_fmac_f32_e32 v191, v195, v195
	v_lshlrev_b32_e32 v194, 16, v181
	v_and_b32_e32 v195, 0xffff0000, v181
	v_fmac_f32_e32 v191, v194, v194
	v_fmac_f32_e32 v191, v195, v195
	v_lshlrev_b32_e32 v194, 16, v182
	v_and_b32_e32 v195, 0xffff0000, v182
	v_fmac_f32_e32 v191, v194, v194
	v_fmac_f32_e32 v191, v195, v195
	v_lshlrev_b32_e32 v194, 16, v183
	v_and_b32_e32 v195, 0xffff0000, v183
	v_fmac_f32_e32 v191, v194, v194
	v_fmac_f32_e32 v191, v195, v195
	s_nop 1
	v_add_f32_dpp v36, v36, v36 quad_perm:[1,0,3,2] row_mask:0xf bank_mask:0xf
	v_add_f32_dpp v37, v37, v37 quad_perm:[1,0,3,2] row_mask:0xf bank_mask:0xf
	v_add_f32_dpp v38, v38, v38 quad_perm:[1,0,3,2] row_mask:0xf bank_mask:0xf
	v_add_f32_dpp v39, v39, v39 quad_perm:[1,0,3,2] row_mask:0xf bank_mask:0xf
	v_add_f32_dpp v40, v40, v40 quad_perm:[1,0,3,2] row_mask:0xf bank_mask:0xf
	v_add_f32_dpp v41, v41, v41 quad_perm:[1,0,3,2] row_mask:0xf bank_mask:0xf
	v_add_f32_dpp v42, v42, v42 quad_perm:[1,0,3,2] row_mask:0xf bank_mask:0xf
	v_add_f32_dpp v43, v43, v43 quad_perm:[1,0,3,2] row_mask:0xf bank_mask:0xf
	v_add_f32_dpp v184, v184, v184 quad_perm:[1,0,3,2] row_mask:0xf bank_mask:0xf
	v_add_f32_dpp v185, v185, v185 quad_perm:[1,0,3,2] row_mask:0xf bank_mask:0xf
	v_add_f32_dpp v186, v186, v186 quad_perm:[1,0,3,2] row_mask:0xf bank_mask:0xf
	v_add_f32_dpp v187, v187, v187 quad_perm:[1,0,3,2] row_mask:0xf bank_mask:0xf
	v_add_f32_dpp v188, v188, v188 quad_perm:[1,0,3,2] row_mask:0xf bank_mask:0xf
	v_add_f32_dpp v189, v189, v189 quad_perm:[1,0,3,2] row_mask:0xf bank_mask:0xf
	v_add_f32_dpp v190, v190, v190 quad_perm:[1,0,3,2] row_mask:0xf bank_mask:0xf
	v_add_f32_dpp v191, v191, v191 quad_perm:[1,0,3,2] row_mask:0xf bank_mask:0xf
	v_add_f32_dpp v36, v36, v36 quad_perm:[2,3,0,1] row_mask:0xf bank_mask:0xf
	v_add_f32_dpp v37, v37, v37 quad_perm:[2,3,0,1] row_mask:0xf bank_mask:0xf
	v_add_f32_dpp v38, v38, v38 quad_perm:[2,3,0,1] row_mask:0xf bank_mask:0xf
	v_add_f32_dpp v39, v39, v39 quad_perm:[2,3,0,1] row_mask:0xf bank_mask:0xf
	v_add_f32_dpp v40, v40, v40 quad_perm:[2,3,0,1] row_mask:0xf bank_mask:0xf
	v_add_f32_dpp v41, v41, v41 quad_perm:[2,3,0,1] row_mask:0xf bank_mask:0xf
	v_add_f32_dpp v42, v42, v42 quad_perm:[2,3,0,1] row_mask:0xf bank_mask:0xf
	v_add_f32_dpp v43, v43, v43 quad_perm:[2,3,0,1] row_mask:0xf bank_mask:0xf
	v_add_f32_dpp v184, v184, v184 quad_perm:[2,3,0,1] row_mask:0xf bank_mask:0xf
	v_add_f32_dpp v185, v185, v185 quad_perm:[2,3,0,1] row_mask:0xf bank_mask:0xf
	v_add_f32_dpp v186, v186, v186 quad_perm:[2,3,0,1] row_mask:0xf bank_mask:0xf
	v_add_f32_dpp v187, v187, v187 quad_perm:[2,3,0,1] row_mask:0xf bank_mask:0xf
	v_add_f32_dpp v188, v188, v188 quad_perm:[2,3,0,1] row_mask:0xf bank_mask:0xf
	v_add_f32_dpp v189, v189, v189 quad_perm:[2,3,0,1] row_mask:0xf bank_mask:0xf
	v_add_f32_dpp v190, v190, v190 quad_perm:[2,3,0,1] row_mask:0xf bank_mask:0xf
	v_add_f32_dpp v191, v191, v191 quad_perm:[2,3,0,1] row_mask:0xf bank_mask:0xf
	v_add_f32_dpp v36, v36, v36 row_half_mirror row_mask:0xf bank_mask:0xf
	v_add_f32_dpp v37, v37, v37 row_half_mirror row_mask:0xf bank_mask:0xf
	v_add_f32_dpp v38, v38, v38 row_half_mirror row_mask:0xf bank_mask:0xf
	v_add_f32_dpp v39, v39, v39 row_half_mirror row_mask:0xf bank_mask:0xf
	v_add_f32_dpp v40, v40, v40 row_half_mirror row_mask:0xf bank_mask:0xf
	v_add_f32_dpp v41, v41, v41 row_half_mirror row_mask:0xf bank_mask:0xf
	v_add_f32_dpp v42, v42, v42 row_half_mirror row_mask:0xf bank_mask:0xf
	v_add_f32_dpp v43, v43, v43 row_half_mirror row_mask:0xf bank_mask:0xf
	v_add_f32_dpp v184, v184, v184 row_half_mirror row_mask:0xf bank_mask:0xf
	v_add_f32_dpp v185, v185, v185 row_half_mirror row_mask:0xf bank_mask:0xf
	v_add_f32_dpp v186, v186, v186 row_half_mirror row_mask:0xf bank_mask:0xf
	v_add_f32_dpp v187, v187, v187 row_half_mirror row_mask:0xf bank_mask:0xf
	v_add_f32_dpp v188, v188, v188 row_half_mirror row_mask:0xf bank_mask:0xf
	v_add_f32_dpp v189, v189, v189 row_half_mirror row_mask:0xf bank_mask:0xf
	v_add_f32_dpp v190, v190, v190 row_half_mirror row_mask:0xf bank_mask:0xf
	v_add_f32_dpp v191, v191, v191 row_half_mirror row_mask:0xf bank_mask:0xf
	s_nop 1
	v_max_f32_e32 v36, v36, v37
	v_max_f32_e32 v38, v38, v39
	v_max_f32_e32 v40, v40, v41
	v_max_f32_e32 v42, v42, v43
	v_max_f32_e32 v184, v184, v185
	v_max_f32_e32 v186, v186, v187
	v_max_f32_e32 v188, v188, v189
	v_max_f32_e32 v190, v190, v191
	v_max_f32_e32 v36, v36, v38
	v_max_f32_e32 v40, v40, v42
	v_max_f32_e32 v184, v184, v186
	v_max_f32_e32 v188, v188, v190
	v_max_f32_e32 v36, v36, v40
	v_max_f32_e32 v184, v184, v188
	v_lshlrev_b32_e32 v4, 2, v1
	v_max_f32_e32 v0, 0, v36
	v_max_f32_e32 v2, 0, v184
	v_xor_b32_e32 v5, 4, v4
	ds_bpermute_b32 v6, v5, v0
	ds_bpermute_b32 v5, v5, v2
	s_waitcnt lgkmcnt(1)
	v_max_f32_e32 v6, v6, v6
	s_waitcnt lgkmcnt(0)
	v_max_f32_e32 v5, v5, v5
	v_max_f32_e32 v0, v0, v6
	v_max_f32_e32 v2, v2, v5
	v_xor_b32_e32 v5, 8, v4
	ds_bpermute_b32 v6, v5, v0
	ds_bpermute_b32 v5, v5, v2
	s_waitcnt lgkmcnt(1)
	v_max_f32_e32 v6, v6, v6
	s_waitcnt lgkmcnt(0)
	v_max_f32_e32 v5, v5, v5
	v_max_f32_e32 v0, v0, v6
	v_max_f32_e32 v2, v2, v5
	v_xor_b32_e32 v5, 16, v4
	ds_bpermute_b32 v6, v5, v0
	ds_bpermute_b32 v5, v5, v2
	s_waitcnt lgkmcnt(1)
	v_max_f32_e32 v6, v6, v6
	s_waitcnt lgkmcnt(0)
	v_max_f32_e32 v5, v5, v5
	v_max_f32_e32 v0, v0, v6
	v_max_f32_e32 v2, v2, v5
	v_xor_b32_e32 v5, 32, v4
	ds_bpermute_b32 v6, v5, v0
	ds_bpermute_b32 v5, v5, v2
	s_waitcnt lgkmcnt(1)
	v_max_f32_e32 v6, v6, v6
	v_max_f32_e32 v0, v0, v6
	s_waitcnt lgkmcnt(0)
	v_max_f32_e32 v5, v5, v5
	v_xor_b32_e32 v6, 64, v4
	v_max_f32_e32 v2, v2, v5
	ds_bpermute_b32 v5, v6, v0
	s_waitcnt lgkmcnt(0)
	v_max_f32_e32 v5, v5, v5
	v_max_f32_e32 v5, v0, v5
	ds_bpermute_b32 v0, v6, v2
	s_waitcnt lgkmcnt(0)
	v_max_f32_e32 v0, v0, v0
	v_max_f32_e32 v2, v2, v0
	v_xor_b32_e32 v0, 0x80, v4
	ds_bpermute_b32 v6, v0, v5
	ds_bpermute_b32 v4, v0, v2
	s_and_saveexec_b64 s[0:1], vcc
	s_cbranch_execz .LBB0_944
	s_waitcnt lgkmcnt(1)
	v_max_f32_e32 v0, v6, v6
	v_max_f32_e32 v1, v5, v5
	s_mov_b64 s[2:3], exec
	v_max_f32_e32 v1, v1, v0
	s_mov_b32 s10, 0
